# attention work queues: next unit index requested one unit ahead (atomic round trip off the critical path), NSA and stick-breaking
# speedup vs baseline: 1.0111x; 1.0111x over previous
.LBB0_501:
	v_mov_b32_e32 v2, v0
	s_add_u32 s6, s70, 0x8000
	s_addc_u32 s7, s71, 0
	v_readfirstlane_b32 s0, v2
	s_ashr_i32 s2, s0, 6
	s_lshl_b32 s20, s2, 5
	s_cmp_lt_i32 s2, 4
	s_cselect_b64 s[0:1], -1, 0
	s_lshl_b32 s29, s2, 10
	s_add_i32 s21, s29, 0
	s_ashr_i32 s3, s29, 31
	v_readlane_b32 s4, v250, 21
	v_readlane_b32 s5, v250, 22
	s_add_u32 s22, s4, s29
	s_addc_u32 s23, s5, s3
	v_readlane_b32 s4, v250, 23
	v_readlane_b32 s5, v250, 24
	s_add_u32 s24, s4, s29
	s_addc_u32 s25, s5, s3
	s_lshl_b32 s3, s2, 2
	s_add_i32 s26, s3, 0
	s_mulk_i32 s2, 0xd00
	s_add_i32 s30, 0, 0x20540
	v_cndmask_b32_e64 v3, 0, 1, s[0:1]
	s_movk_i32 s14, 0xe000
	v_and_b32_e32 v1, 63, v2
	s_add_i32 s26, s26, 0x20500
	s_add_i32 s27, s21, s2
	s_add_i32 s28, s20, 0xffffff40
	s_add_i32 s29, s29, 0x14000
	v_mov_b32_e32 v2, 0
	v_mov_b32_e32 v160, s30
	v_cmp_ne_u32_e64 s[0:1], 1, v3
	s_mov_b64 s[8:9], 0x3e000
	s_mov_b32 s15, -1
	s_add_i32 s31, 0, 0x20500
	v_mov_b32_e32 v161, 0xf149f2ca
	v_mov_b32_e32 v162, 0x3f80
	v_cmp_eq_u32_e32 vcc, 0, v0
	s_and_saveexec_b64 s[2:3], vcc
	s_cbranch_execz .Lsb_wq_pre_done
	v_mov_b32_e32 v248, 1
	global_atomic_add v248, v2, v248, s[6:7] sc0
	s_waitcnt vmcnt(0)
.Lsb_wq_pre_done:
	s_or_b64 exec, exec, s[2:3]
	s_branch .LBB0_504

.LBB0_504:
	v_mov_b32_e32 v3, v0
	s_nop 0
	v_cmp_eq_u32_e32 vcc, 0, v3
	s_barrier
	s_and_saveexec_b64 s[2:3], vcc
	s_cbranch_execz .LBB0_508
	s_waitcnt vmcnt(4)
	v_mov_b32_e32 v3, v248
	v_mov_b32_e32 v4, s30
	ds_write_b32 v4, v3
	v_mov_b32_e32 v248, 1
	global_atomic_add v248, v2, v248, s[6:7] sc0

.LBB0_547:
	s_waitcnt vmcnt(0)
	v_mov_b32_e32 v1, v0
	s_nop 0
	v_readfirstlane_b32 s4, v1
	v_cmp_eq_u32_e32 vcc, 0, v1
	s_barrier
	s_and_saveexec_b64 s[0:1], vcc
	s_cbranch_execz .LBB0_557
	s_mov_b32 s5, 0x400001
	v_mov_b32_e32 v2, 0
	s_branch .LBB0_550

.LBB0_557:
	v_writelane_b32 v250, s82, 37
	v_writelane_b32 v250, s80, 35
	v_writelane_b32 v251, s78, 55
	s_nop 0
	v_writelane_b32 v250, s81, 36
	v_writelane_b32 v250, s77, 34
	v_writelane_b32 v251, s79, 56
	s_or_b64 exec, exec, s[0:1]
	s_add_u32 s0, s70, 0x8100
	s_addc_u32 s1, s71, 0
	s_ashr_i32 s4, s4, 6
	s_and_b32 s3, s4, 3
	v_writelane_b32 v250, s0, 38
	s_cmp_lt_u32 s4, 4
	v_and_b32_e32 v1, 63, v1
	v_writelane_b32 v250, s1, 39
	s_cselect_b64 s[0:1], -1, 0
	s_lshl_b32 s2, s4, 3
	s_and_b32 s6, s2, 0xffffffe0
	s_lshl_b32 s12, s3, 6
	s_mul_i32 s3, s3, 12
	s_add_u32 s13, s10, s3
	s_addc_u32 s14, s11, 0
	s_lshl_b32 s90, s4, 10
	s_lshl_b32 s5, s4, 4
	s_add_i32 s8, s90, 0
	s_and_b32 s15, s5, 48
	s_add_i32 s5, s8, 0x4000
	v_writelane_b32 v250, s5, 40
	s_add_i32 s5, s8, 0x10000
	v_writelane_b32 v250, s5, 42
	s_add_i32 s5, s8, 0x14000
	v_writelane_b32 v250, s5, 43
	s_lshl_b32 s5, s4, 8
	s_add_i32 s5, s5, 0
	s_add_i32 s5, s5, 0x20800
	v_writelane_b32 v250, s5, 44
	s_mul_i32 s5, s4, 0xd00
	s_add_i32 s37, s8, s5
	s_lshl_b32 s5, s4, 5
	s_add_i32 s5, s5, 0x20400
	v_writelane_b32 v250, s5, 45
	s_mulk_i32 s4, 0x420
	v_cndmask_b32_e64 v3, 0, 1, s[0:1]
	v_writelane_b32 v250, s4, 47
	v_cmp_ne_u32_e64 s[0:1], 1, v3
	s_ashr_i32 s3, s2, 31
	s_ashr_i32 s7, s6, 31
	v_writelane_b32 v250, s0, 48
	s_add_i32 s36, s8, 0xc000
	s_or_b32 s34, s15, 64
	v_writelane_b32 v250, s1, 49
	s_lshl_b64 s[0:1], s[2:3], 1
	v_writelane_b32 v250, s0, 50
	s_add_i32 s38, 0, 0x20540
	v_mbcnt_lo_u32_b32 v3, -1, 0
	v_writelane_b32 v250, s1, 51
	v_writelane_b32 v250, s6, 52
	s_lshl_b64 s[0:1], s[6:7], 1
	v_writelane_b32 v249, s36, 0
	v_writelane_b32 v250, s7, 53
	v_writelane_b32 v250, s0, 54
	s_mov_b32 s16, 0
	s_add_i32 s35, s8, 0x8000
	v_writelane_b32 v250, s1, 55
	v_writelane_b32 v250, s62, 56
	s_ashr_i32 s91, s90, 31
	v_mov_b32_e32 v2, 0
	v_writelane_b32 v250, s63, 57
	v_writelane_b32 v250, s12, 58
	v_writelane_b32 v250, s13, 59
	v_writelane_b32 v250, s14, 60
	v_writelane_b32 v250, s15, 61
	v_mov_b32_e32 v194, s38
	s_movk_i32 s39, 0x3ff
	s_add_i32 s33, 0, 0x18000
	s_movk_i32 s64, 0x84
	s_movk_i32 s77, 0x200
	v_mov_b32_e32 v195, 0xf149f2ca
	v_mbcnt_hi_u32_b32 v212, -1, v3
	v_mov_b32_e32 v196, 0x7149f2ca
	v_mov_b32_e32 v197, 0xc2c80000
	v_writelane_b32 v250, s34, 62
	v_writelane_b32 v249, s37, 1
	s_barrier
	v_writelane_b32 v251, s8, 57
	v_writelane_b32 v250, s35, 63
	v_writelane_b32 v249, s38, 2
	v_cmp_eq_u32_e32 vcc, 0, v0
	s_and_saveexec_b64 s[0:1], vcc
	s_cbranch_execz .Lnsa_wq_pre_done
	v_readlane_b32 s4, v250, 38
	v_readlane_b32 s5, v250, 39
	v_mov_b32_e32 v228, 1
	s_nop 4
	global_atomic_add v228, v2, v228, s[4:5] sc0
	s_waitcnt vmcnt(0)
.Lnsa_wq_pre_done:
	s_or_b64 exec, exec, s[0:1]
	s_branch .LBB0_561
.LBB0_558:
	v_readlane_b32 s60, v250, 30
	v_readlane_b32 s94, v250, 13
	v_readlane_b32 s96, v250, 15
	v_readlane_b32 s72, v250, 32
	v_readlane_b32 s62, v250, 56
	v_readlane_b32 s85, v250, 9
	v_readlane_b32 s61, v250, 31
	v_readlane_b32 s95, v250, 14
	v_readlane_b32 s97, v250, 16
	v_readlane_b32 s73, v250, 33
	v_readlane_b32 s63, v250, 57
	v_readlane_b32 s12, v250, 58
	v_readlane_b32 s16, v249, 11
	v_readlane_b32 s13, v250, 59
	v_readlane_b32 s14, v250, 60
	v_readlane_b32 s15, v250, 61
	v_readlane_b32 s34, v250, 62
	v_readlane_b32 s35, v250, 63
	v_readlane_b32 s36, v249, 0
	v_readlane_b32 s37, v249, 1
	v_readlane_b32 s38, v249, 2
	s_movk_i32 s39, 0x3ff
	s_movk_i32 s64, 0x84
	v_readlane_b32 s40, v249, 10
	v_readlane_b32 s17, v249, 12
	v_readlane_b32 s18, v249, 13
	v_readlane_b32 s19, v249, 14
	v_readlane_b32 s20, v249, 15
	v_readlane_b32 s21, v249, 16
	v_readlane_b32 s22, v249, 17
	v_readlane_b32 s23, v249, 18
	v_readlane_b32 s24, v249, 19
	v_readlane_b32 s25, v249, 20
	v_readlane_b32 s26, v249, 21
	v_readlane_b32 s27, v249, 22
	v_readlane_b32 s28, v249, 23
	v_readlane_b32 s29, v249, 24
	v_readlane_b32 s30, v249, 25
	v_readlane_b32 s31, v249, 26

.LBB0_561:
	v_mov_b32_e32 v3, v0
	s_nop 0
	v_cmp_eq_u32_e32 vcc, 0, v3
	s_barrier
	s_and_saveexec_b64 s[0:1], vcc
	s_cbranch_execz .LBB0_565
	v_readlane_b32 s4, v250, 38
	v_readlane_b32 s5, v250, 39
	s_waitcnt vmcnt(4)
	v_mov_b32_e32 v3, v228
	v_mov_b32_e32 v4, s38
	ds_write_b32 v4, v3
	v_mov_b32_e32 v228, 1
	s_nop 1
	global_atomic_add v228, v2, v228, s[4:5] sc0
